# baseline (speedup 1.0000x reference)
.LBB0_37:
	s_or_b64 exec, exec, s[0:1]
	v_mov_b32_e32 v98, v97
	v_mov_b32_e32 v99, v97
	v_mov_b32_e32 v5, v97
	v_mov_b32_e32 v6, v97
	v_mov_b32_e32 v7, v97
	v_mov_b32_e32 v1, v97
	v_mov_b32_e32 v2, v97
	v_mov_b32_e32 v3, v97
	s_mov_b32 s0, 0x10000
	v_or_b32_e32 v8, 0x21000, v223
	v_mfma_f32_32x32x16_f16 v[32:47], v[96:99], v[0:3], 0
	v_mfma_f32_32x32x16_f16 v[16:31], v[4:7], v[0:3], 0
	v_or_b32_e32 v114, 0x21000, v223
	v_cmp_eq_u32_e64 s[0:1], 0, v225
	s_and_b64 vcc, vcc, s[0:1]
	ds_read_b128 v[8:11], v114
	ds_read_b128 v[12:15], v114 offset:32
	ds_read_b128 v[234:237], v114 offset:64
	ds_read_b128 v[238:241], v114 offset:96
	ds_read_b128 v[242:245], v114 offset:128
	ds_read_b128 v[106:109], v114 offset:160
	ds_read_b128 v[110:113], v114 offset:192
	s_waitcnt lgkmcnt(7)
	v_mfma_f32_32x32x16_f16 v[32:47], v[180:183], v[92:95], v[32:47]
	ds_read_b128 v[0:3], v114 offset:224
	v_mfma_f32_32x32x16_f16 v[32:47], v[184:187], v[88:91], v[32:47]
	v_mfma_f32_32x32x16_f16 v[32:47], v[188:191], v[84:87], v[32:47]
	v_mfma_f32_32x32x16_f16 v[32:47], v[192:195], v[80:83], v[32:47]
	v_mfma_f32_32x32x16_f16 v[32:47], v[196:199], v[76:79], v[32:47]
	v_mfma_f32_32x32x16_f16 v[32:47], v[200:203], v[72:75], v[32:47]
	v_mfma_f32_32x32x16_f16 v[32:47], v[204:207], v[68:71], v[32:47]
	v_mfma_f32_32x32x16_f16 v[32:47], v[208:211], v[64:67], v[32:47]
	s_waitcnt lgkmcnt(0)
	v_dot2c_f32_f16_e32 v98, v92, v8
	v_mfma_f32_32x32x16_f16 v[16:31], v[148:151], v[92:95], v[16:31]
	v_dot2c_f32_f16_e32 v98, v93, v9
	v_dot2c_f32_f16_e32 v98, v94, v10
	v_dot2c_f32_f16_e32 v98, v95, v11
	v_dot2c_f32_f16_e32 v98, v88, v12
	v_mfma_f32_32x32x16_f16 v[16:31], v[152:155], v[88:91], v[16:31]
	v_dot2c_f32_f16_e32 v98, v89, v13
	v_dot2c_f32_f16_e32 v98, v90, v14
	v_dot2c_f32_f16_e32 v98, v91, v15
	v_dot2c_f32_f16_e32 v98, v84, v234
	v_mfma_f32_32x32x16_f16 v[16:31], v[156:159], v[84:87], v[16:31]
	v_dot2c_f32_f16_e32 v98, v85, v235
	v_dot2c_f32_f16_e32 v98, v86, v236
	v_dot2c_f32_f16_e32 v98, v87, v237
	v_dot2c_f32_f16_e32 v98, v80, v238
	v_mfma_f32_32x32x16_f16 v[16:31], v[160:163], v[80:83], v[16:31]
	v_dot2c_f32_f16_e32 v98, v81, v239
	v_dot2c_f32_f16_e32 v98, v82, v240
	v_dot2c_f32_f16_e32 v98, v83, v241
	v_dot2c_f32_f16_e32 v98, v76, v242
	v_mfma_f32_32x32x16_f16 v[16:31], v[164:167], v[76:79], v[16:31]
	v_dot2c_f32_f16_e32 v98, v77, v243
	v_dot2c_f32_f16_e32 v98, v78, v244
	v_dot2c_f32_f16_e32 v98, v79, v245
	v_dot2c_f32_f16_e32 v98, v72, v106
	v_mfma_f32_32x32x16_f16 v[16:31], v[168:171], v[72:75], v[16:31]
	v_dot2c_f32_f16_e32 v98, v73, v107
	v_dot2c_f32_f16_e32 v98, v74, v108
	v_dot2c_f32_f16_e32 v98, v75, v109
	v_dot2c_f32_f16_e32 v98, v68, v110
	v_mfma_f32_32x32x16_f16 v[16:31], v[172:175], v[68:71], v[16:31]
	v_dot2c_f32_f16_e32 v98, v69, v111
	v_dot2c_f32_f16_e32 v98, v70, v112
	v_dot2c_f32_f16_e32 v98, v71, v113
	v_cvt_pk_f16_f32 v7, v38, v39
	v_cvt_pk_f16_f32 v6, v36, v37
	v_cvt_pk_f16_f32 v5, v34, v35
	v_cvt_pk_f16_f32 v4, v32, v33
	v_dot2c_f32_f16_e32 v98, v64, v0
	v_dot2c_f32_f16_e32 v98, v65, v1
	v_dot2c_f32_f16_e32 v98, v66, v2
	v_mfma_f32_32x32x16_f16 v[16:31], v[176:179], v[64:67], v[16:31]
	v_dot2c_f32_f16_e32 v98, v67, v3
	v_cvt_pk_f16_f32 v35, v46, v47
	v_cvt_pk_f16_f32 v34, v44, v45
	v_cvt_pk_f16_f32 v33, v42, v43
	v_cvt_pk_f16_f32 v32, v40, v41
	ds_bpermute_b32 v36, v102, v98
	v_cvt_f32_i32_e32 v37, v226
	v_mfma_f32_32x32x16_f16 v[0:15], v[4:7], v[60:63], 0
	s_nop 3
	v_cvt_pk_f16_f32 v23, v22, v23
	v_cvt_pk_f16_f32 v22, v20, v21
	v_cvt_pk_f16_f32 v21, v18, v19
	v_cvt_pk_f16_f32 v20, v16, v17
	v_cvt_pk_f16_f32 v19, v30, v31
	v_cvt_pk_f16_f32 v18, v28, v29
	v_cvt_pk_f16_f32 v17, v26, v27
	v_mfma_f32_32x32x16_f16 v[0:15], v[32:35], v[56:59], v[0:15]
	v_cvt_pk_f16_f32 v16, v24, v25
	s_waitcnt lgkmcnt(0)
	v_add_f32_e32 v36, v98, v36
	v_cvt_f16_f32_e32 v26, v100
	v_mov_b32_e32 v98, v97
	v_lshlrev_b32_e32 v32, 4, v218
	v_mfma_f32_32x32x16_f16 v[0:15], v[20:23], v[52:55], v[0:15]
	v_fma_mixlo_f16 v20, v37, v104, v36
	v_pack_b32_f16 v20, v20, 0
	v_pack_b32_f16 v21, v26, 0
	v_cndmask_b32_e32 v96, 0, v21, vcc
	v_mfma_f32_32x32x16_f16 v[0:15], v[16:19], v[48:51], v[0:15]
	v_cndmask_b32_e32 v16, 0, v20, vcc
	v_mov_b32_e32 v17, v97
	v_mov_b32_e32 v18, v97
	v_mov_b32_e32 v19, v97
	v_cmp_ne_u32_e32 vcc, 0, v225
	s_cmp_lg_u64 s[4:5], 0
	s_cbranch_scc0 .Lz_skip_rank1
	v_mfma_f32_32x32x16_f16 v[0:15], v[16:19], v[96:99], v[0:15]
	v_lshlrev_b32_e32 v70, 2, v215
	v_lshl_add_u32 v70, v214, 4, v70
	global_load_dwordx4 v[16:19], v70, s[64:65]
	global_load_dwordx4 v[20:23], v70, s[64:65] offset:32
	global_load_dwordx4 v[24:27], v70, s[64:65] offset:64
	global_load_dwordx4 v[28:31], v70, s[64:65] offset:96
.Lz_skip_rank1:
	s_and_saveexec_b64 s[6:7], vcc
	s_cbranch_execz .LBB0_39
	v_lshl_or_b32 v71, v251, 12, v32
	v_add_u32_e32 v71, 0x18800, v71
	s_nop 7
	ds_write_b128 v71, v[0:3]
	ds_write_b128 v71, v[4:7] offset:1024
	ds_write_b128 v71, v[8:11] offset:2048
	ds_write_b128 v71, v[12:15] offset:3072
